# layer-1 norm1 MoE-combine: operand loads of column steps 1..5 issued one step earlier (two steps in flight) with counted vmcnt waits
# baseline (speedup 1.0000x reference)
; #define LAS __attribute__((address_space(3)))
; __device__ __forceinline__ float bf_lo(unsigned w) { return __uint_as_float(w << 16); }
; __device__ __forceinline__ float bf_hi(unsigned w) { return __uint_as_float(w & 0xffff0000u); }
; template <int MODE>
; __device__ __forceinline__ void norm_phase(const MkArgs& a, LAS unsigned char* lds, const int l, const int wv) {
;     ...
;             const float w0 = tokw[2 * t], w1 = tokw[2 * t + 1];
; #pragma unroll
;             for (int j = 0; j < 8; ++j) {
;                 const int k = 256 * w + 32 * j + 8 * q;
;                 const u32x4 y0 = *(const u32x4*)(yb + (size_t)(2 * t) * DM + k), y1 = *(const u32x4*)(yb + (size_t)(2 * t + 1) * DM + k);
;                 const f32x4 g0 = *(const LAS f32x4*)&tabG[k], g1 = *(const LAS f32x4*)&tabG[k + 4];
;                 xv[8 * j + 0] += g0[0] * (w0 * bf_lo(y0[0]) + w1 * bf_lo(y1[0])); xv[8 * j + 1] += g0[1] * (w0 * bf_hi(y0[0]) + w1 * bf_hi(y1[0]));
;                 xv[8 * j + 2] += g0[2] * (w0 * bf_lo(y0[1]) + w1 * bf_lo(y1[1])); xv[8 * j + 3] += g0[3] * (w0 * bf_hi(y0[1]) + w1 * bf_hi(y1[1]));
;                 xv[8 * j + 4] += g1[0] * (w0 * bf_lo(y0[2]) + w1 * bf_lo(y1[2])); xv[8 * j + 5] += g1[1] * (w0 * bf_hi(y0[2]) + w1 * bf_hi(y1[2]));
;                 xv[8 * j + 6] += g1[2] * (w0 * bf_lo(y0[3]) + w1 * bf_lo(y1[3])); xv[8 * j + 7] += g1[3] * (w0 * bf_hi(y0[3]) + w1 * bf_hi(y1[3]));
;                 if constexpr (MODE == 1) {
;                     *(f32x4*)(xcur + (size_t)t * DM + k) = (f32x4){xv[8 * j + 0], xv[8 * j + 1], xv[8 * j + 2], xv[8 * j + 3]};
;                     *(f32x4*)(xcur + (size_t)t * DM + k + 4) = (f32x4){xv[8 * j + 4], xv[8 * j + 5], xv[8 * j + 6], xv[8 * j + 7]};
;                 }
;             }
.LBB0_1310:
	v_add_u32_e32 v4, 1, v124
	v_ashrrev_i32_e32 v5, 31, v4
	v_ashrrev_i32_e32 v125, 31, v124
	v_lshlrev_b64 v[4:5], 12, v[4:5]
	v_lshl_add_u64 v[0:1], v[124:125], 2, s[8:9]
	v_lshlrev_b64 v[2:3], 12, v[124:125]
	v_lshl_add_u64 v[62:63], v[112:113], 0, v[4:5]
	v_lshl_add_u64 v[60:61], v[112:113], 0, v[2:3]
	global_load_dwordx2 v[56:57], v[0:1], off
	s_nop 0
	global_load_dwordx4 v[0:3], v[60:61], off
	global_load_dwordx4 v[4:7], v[62:63], off
	v_add_u32_e32 v64, s34, v217
	v_ashrrev_i32_e32 v65, 31, v64
	v_lshlrev_b64 v[8:9], 13, v[64:65]
	v_lshl_add_u64 v[66:67], v[110:111], 0, v[8:9]
	global_load_dwordx4 v[8:11], v[66:67], off
	global_load_dwordx4 v[12:15], v[66:67], off offset:16
	global_load_dwordx4 v[242:245], v[62:63], off offset:64
	global_load_dwordx4 v[246:249], v[60:61], off offset:64
	global_load_dwordx4 v[140:143], v[66:67], off offset:128
	global_load_dwordx4 v[144:147], v[66:67], off offset:144
	ds_read_b128 v[16:19], v176
	ds_read_b128 v[20:23], v176 offset:16
	s_waitcnt vmcnt(8)
	v_pk_mov_b32 v[58:59], v[56:57], v[56:57] op_sel:[1,0]
	s_waitcnt vmcnt(7)
	v_lshlrev_b32_e32 v28, 16, v1
	v_lshlrev_b32_e32 v30, 16, v0
	s_waitcnt vmcnt(6)
	v_and_b32_e32 v29, 0xffff0000, v5
	v_and_b32_e32 v31, 0xffff0000, v4
	v_and_b32_e32 v25, 0xffff0000, v2
	v_lshlrev_b32_e32 v2, 16, v2
	v_and_b32_e32 v27, 0xffff0000, v1
	v_and_b32_e32 v1, 0xffff0000, v0
	v_and_b32_e32 v33, 0xffff0000, v3
	v_lshlrev_b32_e32 v34, 16, v3
	v_lshlrev_b32_e32 v24, 16, v6
	v_and_b32_e32 v3, 0xffff0000, v6
	v_lshlrev_b32_e32 v26, 16, v5
	v_lshlrev_b32_e32 v0, 16, v4
	v_lshlrev_b32_e32 v32, 16, v7
	v_and_b32_e32 v35, 0xffff0000, v7
	v_pk_mul_f32 v[4:5], v[58:59], v[30:31] op_sel:[1,0] op_sel_hi:[0,1]
	v_pk_mul_f32 v[6:7], v[58:59], v[28:29] op_sel:[1,0] op_sel_hi:[0,1]
	v_pk_mul_f32 v[2:3], v[58:59], v[2:3] op_sel:[1,0] op_sel_hi:[0,1]
	v_pk_mul_f32 v[28:29], v[58:59], v[34:35] op_sel:[1,0] op_sel_hi:[0,1]
	v_pk_fma_f32 v[0:1], v[56:57], v[0:1], v[4:5] op_sel:[1,0,0] op_sel_hi:[0,1,1]
	v_pk_fma_f32 v[6:7], v[56:57], v[26:27], v[6:7] op_sel:[1,0,0] op_sel_hi:[0,1,1]
	v_pk_fma_f32 v[2:3], v[56:57], v[24:25], v[2:3] op_sel:[1,0,0] op_sel_hi:[0,1,1]
	v_pk_fma_f32 v[24:25], v[56:57], v[32:33], v[28:29] op_sel:[1,0,0] op_sel_hi:[0,1,1]
	s_waitcnt vmcnt(5) lgkmcnt(1)
	v_pk_fma_f32 v[4:5], v[16:17], v[0:1], v[8:9]
	v_pk_fma_f32 v[6:7], v[18:19], v[6:7], v[10:11]
	s_waitcnt vmcnt(4) lgkmcnt(0)
	v_pk_fma_f32 v[0:1], v[20:21], v[2:3], v[12:13]
	v_pk_fma_f32 v[2:3], v[22:23], v[24:25], v[14:15]
	global_store_dwordx4 v[66:67], v[4:7], off
	global_store_dwordx4 v[66:67], v[0:3], off offset:16
	global_load_dwordx4 v[226:229], v[62:63], off offset:128
	global_load_dwordx4 v[230:233], v[60:61], off offset:128
	global_load_dwordx4 v[234:237], v[66:67], off offset:256
	global_load_dwordx4 v[238:241], v[66:67], off offset:272
	ds_read_b128 v[24:27], v177
	ds_read_b128 v[28:31], v177 offset:16
	v_pk_mul_f32 v[154:155], v[4:5], v[4:5]
	v_pk_mul_f32 v[156:157], v[6:7], v[6:7]
	v_add_f32_e32 v116, v154, v155
	v_add_f32_e32 v116, v156, v116
	v_pk_mul_f32 v[158:159], v[0:1], v[0:1]
	v_add_f32_e32 v116, v157, v116
	v_add_f32_e32 v116, v158, v116
	v_add_f32_e32 v116, v159, v116
	s_waitcnt vmcnt(9)
	v_and_b32_e32 v39, 0xffff0000, v243
	s_waitcnt vmcnt(8)
	v_and_b32_e32 v37, 0xffff0000, v247
	v_lshlrev_b32_e32 v38, 16, v247
	v_and_b32_e32 v41, 0xffff0000, v246
	v_lshlrev_b32_e32 v12, 16, v246
	v_and_b32_e32 v13, 0xffff0000, v242
	v_lshlrev_b32_e32 v32, 16, v244
	v_and_b32_e32 v33, 0xffff0000, v248
	v_lshlrev_b32_e32 v34, 16, v248
	v_and_b32_e32 v35, 0xffff0000, v244
	v_lshlrev_b32_e32 v36, 16, v243
	v_lshlrev_b32_e32 v40, 16, v242
	v_lshlrev_b32_e32 v8, 16, v245
	v_and_b32_e32 v9, 0xffff0000, v249
	v_lshlrev_b32_e32 v10, 16, v249
	v_and_b32_e32 v11, 0xffff0000, v245
	v_pk_mul_f32 v[12:13], v[58:59], v[12:13] op_sel:[1,0] op_sel_hi:[0,1]
	v_pk_mul_f32 v[14:15], v[58:59], v[38:39] op_sel:[1,0] op_sel_hi:[0,1]
	v_pk_mul_f32 v[34:35], v[58:59], v[34:35] op_sel:[1,0] op_sel_hi:[0,1]
	v_pk_mul_f32 v[10:11], v[58:59], v[10:11] op_sel:[1,0] op_sel_hi:[0,1]
	v_pk_fma_f32 v[12:13], v[56:57], v[40:41], v[12:13] op_sel:[1,0,0] op_sel_hi:[0,1,1]
	v_pk_fma_f32 v[14:15], v[56:57], v[36:37], v[14:15] op_sel:[1,0,0] op_sel_hi:[0,1,1]
	v_pk_fma_f32 v[32:33], v[56:57], v[32:33], v[34:35] op_sel:[1,0,0] op_sel_hi:[0,1,1]
	v_pk_fma_f32 v[10:11], v[56:57], v[8:9], v[10:11] op_sel:[1,0,0] op_sel_hi:[0,1,1]
	s_waitcnt vmcnt(7) lgkmcnt(1)
	v_pk_fma_f32 v[12:13], v[24:25], v[12:13], v[140:141]
	v_pk_fma_f32 v[14:15], v[26:27], v[14:15], v[142:143]
	s_waitcnt vmcnt(6) lgkmcnt(0)
	v_pk_fma_f32 v[8:9], v[28:29], v[32:33], v[144:145]
	v_pk_fma_f32 v[10:11], v[30:31], v[10:11], v[146:147]
	global_store_dwordx4 v[66:67], v[12:15], off offset:128
	global_store_dwordx4 v[66:67], v[8:11], off offset:144
	global_load_dwordx4 v[242:245], v[62:63], off offset:192
	global_load_dwordx4 v[246:249], v[60:61], off offset:192
	global_load_dwordx4 v[140:143], v[66:67], off offset:384
	global_load_dwordx4 v[144:147], v[66:67], off offset:400
	ds_read_b128 v[32:35], v178
	ds_read_b128 v[36:39], v178 offset:16
	s_waitcnt vmcnt(9)
	v_and_b32_e32 v47, 0xffff0000, v227
	s_waitcnt vmcnt(8)
; #define LAS __attribute__((address_space(3)))
; __device__ __forceinline__ float bf_lo(unsigned w) { return __uint_as_float(w << 16); }
; __device__ __forceinline__ float bf_hi(unsigned w) { return __uint_as_float(w & 0xffff0000u); }
; template <int MODE>
; __device__ __forceinline__ void norm_phase(const MkArgs& a, LAS unsigned char* lds, const int l, const int wv) {
;     ...
;             for (int j = 0; j < 8; ++j) {
;                 const int k = 256 * w + 32 * j + 8 * q;
;                 const u32x4 y0 = *(const u32x4*)(yb + (size_t)(2 * t) * DM + k), y1 = *(const u32x4*)(yb + (size_t)(2 * t + 1) * DM + k);
;                 const f32x4 g0 = *(const LAS f32x4*)&tabG[k], g1 = *(const LAS f32x4*)&tabG[k + 4];
;                 xv[8 * j + 0] += g0[0] * (w0 * bf_lo(y0[0]) + w1 * bf_lo(y1[0])); xv[8 * j + 1] += g0[1] * (w0 * bf_hi(y0[0]) + w1 * bf_hi(y1[0]));
;                 xv[8 * j + 2] += g0[2] * (w0 * bf_lo(y0[1]) + w1 * bf_lo(y1[1])); xv[8 * j + 3] += g0[3] * (w0 * bf_hi(y0[1]) + w1 * bf_hi(y1[1]));
;                 xv[8 * j + 4] += g1[0] * (w0 * bf_lo(y0[2]) + w1 * bf_lo(y1[2])); xv[8 * j + 5] += g1[1] * (w0 * bf_hi(y0[2]) + w1 * bf_hi(y1[2]));
;                 xv[8 * j + 6] += g1[2] * (w0 * bf_lo(y0[3]) + w1 * bf_lo(y1[3])); xv[8 * j + 7] += g1[3] * (w0 * bf_hi(y0[3]) + w1 * bf_hi(y1[3]));
;                 if constexpr (MODE == 1) {
;                     *(f32x4*)(xcur + (size_t)t * DM + k) = (f32x4){xv[8 * j + 0], xv[8 * j + 1], xv[8 * j + 2], xv[8 * j + 3]};
;                     *(f32x4*)(xcur + (size_t)t * DM + k + 4) = (f32x4){xv[8 * j + 4], xv[8 * j + 5], xv[8 * j + 6], xv[8 * j + 7]};
;                 }
;             }
	v_and_b32_e32 v45, 0xffff0000, v231
	v_lshlrev_b32_e32 v46, 16, v231
	v_and_b32_e32 v49, 0xffff0000, v230
	v_lshlrev_b32_e32 v20, 16, v230
	v_and_b32_e32 v21, 0xffff0000, v226
	v_lshlrev_b32_e32 v40, 16, v228
	v_and_b32_e32 v41, 0xffff0000, v232
	v_lshlrev_b32_e32 v42, 16, v232
	v_and_b32_e32 v43, 0xffff0000, v228
	v_lshlrev_b32_e32 v44, 16, v227
	v_lshlrev_b32_e32 v48, 16, v226
	v_lshlrev_b32_e32 v16, 16, v229
	v_and_b32_e32 v17, 0xffff0000, v233
	v_lshlrev_b32_e32 v18, 16, v233
	v_and_b32_e32 v19, 0xffff0000, v229
	v_pk_mul_f32 v[20:21], v[58:59], v[20:21] op_sel:[1,0] op_sel_hi:[0,1]
	v_pk_mul_f32 v[22:23], v[58:59], v[46:47] op_sel:[1,0] op_sel_hi:[0,1]
	v_pk_mul_f32 v[42:43], v[58:59], v[42:43] op_sel:[1,0] op_sel_hi:[0,1]
	v_pk_mul_f32 v[18:19], v[58:59], v[18:19] op_sel:[1,0] op_sel_hi:[0,1]
	v_pk_fma_f32 v[20:21], v[56:57], v[48:49], v[20:21] op_sel:[1,0,0] op_sel_hi:[0,1,1]
	v_pk_fma_f32 v[22:23], v[56:57], v[44:45], v[22:23] op_sel:[1,0,0] op_sel_hi:[0,1,1]
	v_pk_fma_f32 v[40:41], v[56:57], v[40:41], v[42:43] op_sel:[1,0,0] op_sel_hi:[0,1,1]
	v_pk_fma_f32 v[18:19], v[56:57], v[16:17], v[18:19] op_sel:[1,0,0] op_sel_hi:[0,1,1]
	s_waitcnt vmcnt(7) lgkmcnt(1)
	v_pk_fma_f32 v[20:21], v[32:33], v[20:21], v[234:235]
	v_pk_fma_f32 v[22:23], v[34:35], v[22:23], v[236:237]
	s_waitcnt vmcnt(6) lgkmcnt(0)
	v_pk_fma_f32 v[16:17], v[36:37], v[40:41], v[238:239]
	v_pk_fma_f32 v[18:19], v[38:39], v[18:19], v[240:241]
	global_store_dwordx4 v[66:67], v[20:23], off offset:256
	global_store_dwordx4 v[66:67], v[16:19], off offset:272
	global_load_dwordx4 v[226:229], v[62:63], off offset:256
	global_load_dwordx4 v[230:233], v[60:61], off offset:256
	global_load_dwordx4 v[234:237], v[66:67], off offset:512
	global_load_dwordx4 v[238:241], v[66:67], off offset:528
	ds_read_b128 v[40:43], v179
	ds_read_b128 v[44:47], v179 offset:16
	s_waitcnt vmcnt(9)
	v_and_b32_e32 v55, 0xffff0000, v243
	s_waitcnt vmcnt(8)
	v_and_b32_e32 v53, 0xffff0000, v247
	v_lshlrev_b32_e32 v54, 16, v247
	v_and_b32_e32 v69, 0xffff0000, v246
	v_lshlrev_b32_e32 v28, 16, v246
	v_and_b32_e32 v29, 0xffff0000, v242
	v_lshlrev_b32_e32 v48, 16, v244
	v_and_b32_e32 v49, 0xffff0000, v248
	v_lshlrev_b32_e32 v50, 16, v248
	v_and_b32_e32 v51, 0xffff0000, v244
	v_lshlrev_b32_e32 v52, 16, v243
	v_lshlrev_b32_e32 v68, 16, v242
	v_lshlrev_b32_e32 v24, 16, v245
	v_and_b32_e32 v25, 0xffff0000, v249
	v_lshlrev_b32_e32 v26, 16, v249
	v_and_b32_e32 v27, 0xffff0000, v245
	v_pk_mul_f32 v[28:29], v[58:59], v[28:29] op_sel:[1,0] op_sel_hi:[0,1]
	v_pk_mul_f32 v[30:31], v[58:59], v[54:55] op_sel:[1,0] op_sel_hi:[0,1]
	v_pk_mul_f32 v[50:51], v[58:59], v[50:51] op_sel:[1,0] op_sel_hi:[0,1]
	v_pk_mul_f32 v[26:27], v[58:59], v[26:27] op_sel:[1,0] op_sel_hi:[0,1]
	v_pk_fma_f32 v[28:29], v[56:57], v[68:69], v[28:29] op_sel:[1,0,0] op_sel_hi:[0,1,1]
	v_pk_fma_f32 v[30:31], v[56:57], v[52:53], v[30:31] op_sel:[1,0,0] op_sel_hi:[0,1,1]
	v_pk_fma_f32 v[48:49], v[56:57], v[48:49], v[50:51] op_sel:[1,0,0] op_sel_hi:[0,1,1]
	v_pk_fma_f32 v[26:27], v[56:57], v[24:25], v[26:27] op_sel:[1,0,0] op_sel_hi:[0,1,1]
	s_waitcnt vmcnt(7) lgkmcnt(1)
	v_pk_fma_f32 v[28:29], v[40:41], v[28:29], v[140:141]
	v_pk_fma_f32 v[30:31], v[42:43], v[30:31], v[142:143]
	s_waitcnt vmcnt(6) lgkmcnt(0)
	v_pk_fma_f32 v[24:25], v[44:45], v[48:49], v[144:145]
	v_pk_fma_f32 v[26:27], v[46:47], v[26:27], v[146:147]
	global_store_dwordx4 v[66:67], v[28:31], off offset:384
	global_store_dwordx4 v[66:67], v[24:27], off offset:400
	global_load_dwordx4 v[242:245], v[62:63], off offset:320
	global_load_dwordx4 v[246:249], v[60:61], off offset:320
	global_load_dwordx4 v[140:143], v[66:67], off offset:640
	global_load_dwordx4 v[144:147], v[66:67], off offset:656
	ds_read_b128 v[48:51], v180
	ds_read_b128 v[52:55], v180 offset:16
	s_waitcnt vmcnt(9)
	v_and_b32_e32 v129, 0xffff0000, v227
	s_waitcnt vmcnt(8)
	v_and_b32_e32 v127, 0xffff0000, v231
	v_lshlrev_b32_e32 v128, 16, v231
	v_and_b32_e32 v131, 0xffff0000, v230
	v_lshlrev_b32_e32 v36, 16, v230
	v_and_b32_e32 v37, 0xffff0000, v226
	v_lshlrev_b32_e32 v68, 16, v228
	v_and_b32_e32 v69, 0xffff0000, v232
	v_lshlrev_b32_e32 v70, 16, v232
	v_and_b32_e32 v71, 0xffff0000, v228
	v_lshlrev_b32_e32 v126, 16, v227
	v_lshlrev_b32_e32 v130, 16, v226
	v_lshlrev_b32_e32 v32, 16, v229
	v_and_b32_e32 v33, 0xffff0000, v233
	v_lshlrev_b32_e32 v34, 16, v233
	v_and_b32_e32 v35, 0xffff0000, v229
	v_pk_mul_f32 v[36:37], v[58:59], v[36:37] op_sel:[1,0] op_sel_hi:[0,1]
	v_pk_mul_f32 v[38:39], v[58:59], v[128:129] op_sel:[1,0] op_sel_hi:[0,1]
	v_pk_mul_f32 v[70:71], v[58:59], v[70:71] op_sel:[1,0] op_sel_hi:[0,1]
	v_pk_mul_f32 v[34:35], v[58:59], v[34:35] op_sel:[1,0] op_sel_hi:[0,1]
	v_pk_fma_f32 v[36:37], v[56:57], v[130:131], v[36:37] op_sel:[1,0,0] op_sel_hi:[0,1,1]
	v_pk_fma_f32 v[38:39], v[56:57], v[126:127], v[38:39] op_sel:[1,0,0] op_sel_hi:[0,1,1]
	v_pk_fma_f32 v[68:69], v[56:57], v[68:69], v[70:71] op_sel:[1,0,0] op_sel_hi:[0,1,1]
	v_pk_fma_f32 v[34:35], v[56:57], v[32:33], v[34:35] op_sel:[1,0,0] op_sel_hi:[0,1,1]
	s_waitcnt vmcnt(7) lgkmcnt(1)
	v_pk_fma_f32 v[36:37], v[48:49], v[36:37], v[234:235]
	v_pk_fma_f32 v[38:39], v[50:51], v[38:39], v[236:237]
	s_waitcnt vmcnt(6) lgkmcnt(0)
	v_pk_fma_f32 v[32:33], v[52:53], v[68:69], v[238:239]
	v_pk_fma_f32 v[34:35], v[54:55], v[34:35], v[240:241]
	global_store_dwordx4 v[66:67], v[36:39], off offset:512
	global_store_dwordx4 v[66:67], v[32:35], off offset:528
	ds_read_b128 v[68:71], v181
	ds_read_b128 v[126:129], v181 offset:16
	s_waitcnt vmcnt(5)
	v_and_b32_e32 v137, 0xffff0000, v243
	s_waitcnt vmcnt(4)
; #define LAS __attribute__((address_space(3)))
; __device__ __forceinline__ float bf_lo(unsigned w) { return __uint_as_float(w << 16); }
; __device__ __forceinline__ float bf_hi(unsigned w) { return __uint_as_float(w & 0xffff0000u); }
; template <int MODE>
; __device__ __forceinline__ void norm_phase(const MkArgs& a, LAS unsigned char* lds, const int l, const int wv) {
;     ...
;             for (int j = 0; j < 8; ++j) {
;                 const int k = 256 * w + 32 * j + 8 * q;
;                 const u32x4 y0 = *(const u32x4*)(yb + (size_t)(2 * t) * DM + k), y1 = *(const u32x4*)(yb + (size_t)(2 * t + 1) * DM + k);
;                 const f32x4 g0 = *(const LAS f32x4*)&tabG[k], g1 = *(const LAS f32x4*)&tabG[k + 4];
;                 xv[8 * j + 0] += g0[0] * (w0 * bf_lo(y0[0]) + w1 * bf_lo(y1[0])); xv[8 * j + 1] += g0[1] * (w0 * bf_hi(y0[0]) + w1 * bf_hi(y1[0]));
;                 xv[8 * j + 2] += g0[2] * (w0 * bf_lo(y0[1]) + w1 * bf_lo(y1[1])); xv[8 * j + 3] += g0[3] * (w0 * bf_hi(y0[1]) + w1 * bf_hi(y1[1]));
;                 xv[8 * j + 4] += g1[0] * (w0 * bf_lo(y0[2]) + w1 * bf_lo(y1[2])); xv[8 * j + 5] += g1[1] * (w0 * bf_hi(y0[2]) + w1 * bf_hi(y1[2]));
;                 xv[8 * j + 6] += g1[2] * (w0 * bf_lo(y0[3]) + w1 * bf_lo(y1[3])); xv[8 * j + 7] += g1[3] * (w0 * bf_hi(y0[3]) + w1 * bf_hi(y1[3]));
;                 if constexpr (MODE == 1) {
;                     *(f32x4*)(xcur + (size_t)t * DM + k) = (f32x4){xv[8 * j + 0], xv[8 * j + 1], xv[8 * j + 2], xv[8 * j + 3]};
;                     *(f32x4*)(xcur + (size_t)t * DM + k + 4) = (f32x4){xv[8 * j + 4], xv[8 * j + 5], xv[8 * j + 6], xv[8 * j + 7]};
;                 }
;             }
	v_and_b32_e32 v135, 0xffff0000, v247
	v_lshlrev_b32_e32 v136, 16, v247
	v_and_b32_e32 v139, 0xffff0000, v246
	v_lshlrev_b32_e32 v44, 16, v246
	v_and_b32_e32 v45, 0xffff0000, v242
	v_lshlrev_b32_e32 v130, 16, v244
	v_and_b32_e32 v131, 0xffff0000, v248
	v_lshlrev_b32_e32 v132, 16, v248
	v_and_b32_e32 v133, 0xffff0000, v244
	v_lshlrev_b32_e32 v134, 16, v243
	v_lshlrev_b32_e32 v138, 16, v242
	v_lshlrev_b32_e32 v40, 16, v245
	v_and_b32_e32 v41, 0xffff0000, v249
	v_lshlrev_b32_e32 v42, 16, v249
	v_and_b32_e32 v43, 0xffff0000, v245
	v_pk_mul_f32 v[44:45], v[58:59], v[44:45] op_sel:[1,0] op_sel_hi:[0,1]
	v_pk_mul_f32 v[46:47], v[58:59], v[136:137] op_sel:[1,0] op_sel_hi:[0,1]
	v_pk_mul_f32 v[132:133], v[58:59], v[132:133] op_sel:[1,0] op_sel_hi:[0,1]
	v_pk_mul_f32 v[42:43], v[58:59], v[42:43] op_sel:[1,0] op_sel_hi:[0,1]
	v_pk_fma_f32 v[44:45], v[56:57], v[138:139], v[44:45] op_sel:[1,0,0] op_sel_hi:[0,1,1]
	v_pk_fma_f32 v[46:47], v[56:57], v[134:135], v[46:47] op_sel:[1,0,0] op_sel_hi:[0,1,1]
	v_pk_fma_f32 v[130:131], v[56:57], v[130:131], v[132:133] op_sel:[1,0,0] op_sel_hi:[0,1,1]
	v_pk_fma_f32 v[42:43], v[56:57], v[40:41], v[42:43] op_sel:[1,0,0] op_sel_hi:[0,1,1]
	s_waitcnt vmcnt(3) lgkmcnt(1)
	v_pk_fma_f32 v[44:45], v[68:69], v[44:45], v[140:141]
	v_pk_fma_f32 v[46:47], v[70:71], v[46:47], v[142:143]
	s_waitcnt vmcnt(2) lgkmcnt(0)
	v_pk_fma_f32 v[40:41], v[126:127], v[130:131], v[144:145]
	v_pk_fma_f32 v[42:43], v[128:129], v[42:43], v[146:147]
	global_store_dwordx4 v[66:67], v[44:47], off offset:640
	global_store_dwordx4 v[66:67], v[40:43], off offset:656
	global_load_dwordx4 v[48:51], v[62:63], off offset:384
	global_load_dwordx4 v[52:55], v[60:61], off offset:384
	global_load_dwordx4 v[68:71], v[66:67], off offset:768
	global_load_dwordx4 v[126:129], v[66:67], off offset:784
	ds_read_b128 v[130:133], v182
	ds_read_b128 v[134:137], v182 offset:16
	ds_read_b128 v[138:141], v183
	ds_read_b128 v[142:145], v183 offset:16
	global_load_dwordx4 v[146:149], v[66:67], off offset:912
	global_load_dwordx4 v[150:153], v[66:67], off offset:896
	s_waitcnt vmcnt(5)
	v_and_b32_e32 v167, 0xffff0000, v49
	s_waitcnt vmcnt(4)
	v_and_b32_e32 v165, 0xffff0000, v53
	v_lshlrev_b32_e32 v166, 16, v53
	v_and_b32_e32 v225, 0xffff0000, v52
	v_lshlrev_b32_e32 v52, 16, v52
	v_and_b32_e32 v53, 0xffff0000, v48
	v_lshlrev_b32_e32 v160, 16, v50
	v_and_b32_e32 v161, 0xffff0000, v54
	v_lshlrev_b32_e32 v162, 16, v54
	v_and_b32_e32 v163, 0xffff0000, v50
	v_lshlrev_b32_e32 v164, 16, v49
	v_lshlrev_b32_e32 v224, 16, v48
	v_lshlrev_b32_e32 v48, 16, v51
	v_and_b32_e32 v49, 0xffff0000, v55
	v_lshlrev_b32_e32 v50, 16, v55
	v_and_b32_e32 v51, 0xffff0000, v51
	v_pk_mul_f32 v[52:53], v[58:59], v[52:53] op_sel:[1,0] op_sel_hi:[0,1]
	v_pk_mul_f32 v[54:55], v[58:59], v[166:167] op_sel:[1,0] op_sel_hi:[0,1]
	v_pk_mul_f32 v[162:163], v[58:59], v[162:163] op_sel:[1,0] op_sel_hi:[0,1]
	v_pk_mul_f32 v[50:51], v[58:59], v[50:51] op_sel:[1,0] op_sel_hi:[0,1]
	v_pk_fma_f32 v[52:53], v[56:57], v[224:225], v[52:53] op_sel:[1,0,0] op_sel_hi:[0,1,1]
	v_pk_fma_f32 v[54:55], v[56:57], v[164:165], v[54:55] op_sel:[1,0,0] op_sel_hi:[0,1,1]
	v_pk_fma_f32 v[160:161], v[56:57], v[160:161], v[162:163] op_sel:[1,0,0] op_sel_hi:[0,1,1]
	v_pk_fma_f32 v[50:51], v[56:57], v[48:49], v[50:51] op_sel:[1,0,0] op_sel_hi:[0,1,1]
	s_waitcnt vmcnt(3) lgkmcnt(3)
	v_pk_fma_f32 v[52:53], v[130:131], v[52:53], v[68:69]
	v_pk_fma_f32 v[54:55], v[132:133], v[54:55], v[70:71]
	s_waitcnt vmcnt(2) lgkmcnt(2)
; #define LAS __attribute__((address_space(3)))
; __device__ __forceinline__ float bf_lo(unsigned w) { return __uint_as_float(w << 16); }
; __device__ __forceinline__ float bf_hi(unsigned w) { return __uint_as_float(w & 0xffff0000u); }
; template <int MODE>
; __device__ __forceinline__ void norm_phase(const MkArgs& a, LAS unsigned char* lds, const int l, const int wv) {
;     ...
;             for (int j = 0; j < 8; ++j) {
;                 const int k = 256 * w + 32 * j + 8 * q;
;                 const u32x4 y0 = *(const u32x4*)(yb + (size_t)(2 * t) * DM + k), y1 = *(const u32x4*)(yb + (size_t)(2 * t + 1) * DM + k);
;                 const f32x4 g0 = *(const LAS f32x4*)&tabG[k], g1 = *(const LAS f32x4*)&tabG[k + 4];
;                 xv[8 * j + 0] += g0[0] * (w0 * bf_lo(y0[0]) + w1 * bf_lo(y1[0])); xv[8 * j + 1] += g0[1] * (w0 * bf_hi(y0[0]) + w1 * bf_hi(y1[0]));
;                 xv[8 * j + 2] += g0[2] * (w0 * bf_lo(y0[1]) + w1 * bf_lo(y1[1])); xv[8 * j + 3] += g0[3] * (w0 * bf_hi(y0[1]) + w1 * bf_hi(y1[1]));
;                 xv[8 * j + 4] += g1[0] * (w0 * bf_lo(y0[2]) + w1 * bf_lo(y1[2])); xv[8 * j + 5] += g1[1] * (w0 * bf_hi(y0[2]) + w1 * bf_hi(y1[2]));
;                 xv[8 * j + 6] += g1[2] * (w0 * bf_lo(y0[3]) + w1 * bf_lo(y1[3])); xv[8 * j + 7] += g1[3] * (w0 * bf_hi(y0[3]) + w1 * bf_hi(y1[3]));
;                 if constexpr (MODE == 1) {
;                     *(f32x4*)(xcur + (size_t)t * DM + k) = (f32x4){xv[8 * j + 0], xv[8 * j + 1], xv[8 * j + 2], xv[8 * j + 3]};
;                     *(f32x4*)(xcur + (size_t)t * DM + k + 4) = (f32x4){xv[8 * j + 4], xv[8 * j + 5], xv[8 * j + 6], xv[8 * j + 7]};
;                 }
;             }
;         }
;         float ss = 0.f;
; #pragma unroll
;         for (int i = 0; i < 64; ++i) ss += xv[i] * xv[i];
;         ss += __shfl_xor(ss, 16); ss += __shfl_xor(ss, 32);
;         if (q == 0) ssp[w * 16 + r] = ss;
	v_pk_fma_f32 v[48:49], v[134:135], v[160:161], v[126:127]
	v_pk_fma_f32 v[50:51], v[136:137], v[50:51], v[128:129]
	global_store_dwordx4 v[66:67], v[52:55], off offset:768
	global_store_dwordx4 v[66:67], v[48:51], off offset:784
	global_load_dwordx4 v[68:71], v[60:61], off offset:448
	s_nop 0
	global_load_dwordx4 v[60:63], v[62:63], off offset:448
	v_pk_mul_f32 v[126:127], v[2:3], v[2:3]
	v_pk_mul_f32 v[128:129], v[14:15], v[14:15]
	v_add_f32_e32 v116, v126, v116
	v_add_f32_e32 v116, v127, v116
	v_pk_mul_f32 v[126:127], v[12:13], v[12:13]
	v_pk_mul_f32 v[130:131], v[8:9], v[8:9]
	v_add_f32_e32 v116, v126, v116
	v_add_f32_e32 v116, v127, v116
	v_add_f32_e32 v116, v128, v116
	v_add_f32_e32 v116, v129, v116
	v_add_f32_e32 v116, v130, v116
	v_pk_mul_f32 v[132:133], v[10:11], v[10:11]
	v_add_f32_e32 v116, v131, v116
	v_add_f32_e32 v116, v132, v116
	v_add_f32_e32 v116, v133, v116
	v_pk_mul_f32 v[126:127], v[20:21], v[20:21]
	v_pk_mul_f32 v[128:129], v[22:23], v[22:23]
	v_add_f32_e32 v116, v126, v116
	v_add_f32_e32 v116, v127, v116
	v_add_f32_e32 v116, v128, v116
	v_pk_mul_f32 v[130:131], v[16:17], v[16:17]
	v_add_f32_e32 v116, v129, v116
	v_add_f32_e32 v116, v130, v116
	v_pk_mul_f32 v[132:133], v[18:19], v[18:19]
	v_add_f32_e32 v116, v131, v116
	v_add_f32_e32 v116, v132, v116
	v_add_f32_e32 v116, v133, v116
	v_pk_mul_f32 v[126:127], v[28:29], v[28:29]
	v_pk_mul_f32 v[128:129], v[30:31], v[30:31]
	v_add_f32_e32 v116, v126, v116
	v_add_f32_e32 v116, v127, v116
	v_add_f32_e32 v116, v128, v116
	v_pk_mul_f32 v[130:131], v[24:25], v[24:25]
	v_add_f32_e32 v116, v129, v116
	v_add_f32_e32 v116, v130, v116
	v_pk_mul_f32 v[132:133], v[26:27], v[26:27]
	v_add_f32_e32 v116, v131, v116
	v_add_f32_e32 v116, v132, v116
	v_add_f32_e32 v116, v133, v116
	v_pk_mul_f32 v[126:127], v[36:37], v[36:37]
	v_pk_mul_f32 v[128:129], v[38:39], v[38:39]
	v_add_f32_e32 v116, v126, v116
	v_add_f32_e32 v116, v127, v116
	v_add_f32_e32 v116, v128, v116
	v_pk_mul_f32 v[130:131], v[32:33], v[32:33]
	v_add_f32_e32 v116, v129, v116
	v_add_f32_e32 v116, v130, v116
	v_pk_mul_f32 v[132:133], v[34:35], v[34:35]
	v_add_f32_e32 v116, v131, v116
	v_add_f32_e32 v116, v132, v116
	v_add_f32_e32 v116, v133, v116
	v_pk_mul_f32 v[126:127], v[44:45], v[44:45]
	v_pk_mul_f32 v[128:129], v[46:47], v[46:47]
	v_add_f32_e32 v116, v126, v116
	v_add_f32_e32 v116, v127, v116
	v_add_f32_e32 v116, v128, v116
	v_pk_mul_f32 v[130:131], v[40:41], v[40:41]
	v_add_f32_e32 v116, v129, v116
	v_add_f32_e32 v116, v130, v116
	v_pk_mul_f32 v[132:133], v[42:43], v[42:43]
	v_add_f32_e32 v116, v131, v116
	v_add_f32_e32 v116, v132, v116
	v_add_f32_e32 v116, v133, v116
	v_pk_mul_f32 v[126:127], v[52:53], v[52:53]
	v_pk_mul_f32 v[128:129], v[54:55], v[54:55]
	v_add_f32_e32 v116, v126, v116
	v_add_f32_e32 v116, v127, v116
	v_add_f32_e32 v116, v128, v116
	v_pk_mul_f32 v[130:131], v[48:49], v[48:49]
	v_add_f32_e32 v116, v129, v116
	v_add_f32_e32 v116, v130, v116
	v_add_f32_e32 v116, v131, v116
	v_pk_mul_f32 v[132:133], v[50:51], v[50:51]
	s_waitcnt vmcnt(1)
	v_and_b32_e32 v131, 0xffff0000, v69
	v_lshlrev_b32_e32 v134, 16, v69
	v_and_b32_e32 v137, 0xffff0000, v68
	v_lshlrev_b32_e32 v68, 16, v68
	s_waitcnt vmcnt(0)
	v_and_b32_e32 v69, 0xffff0000, v60
	v_lshlrev_b32_e32 v126, 16, v62
	v_lshlrev_b32_e32 v128, 16, v70
	v_and_b32_e32 v129, 0xffff0000, v62
	v_and_b32_e32 v135, 0xffff0000, v61
	v_lshlrev_b32_e32 v136, 16, v60
	v_lshlrev_b32_e32 v60, 16, v63
	v_lshlrev_b32_e32 v62, 16, v71
	v_and_b32_e32 v63, 0xffff0000, v63
	v_pk_mul_f32 v[68:69], v[58:59], v[68:69] op_sel:[1,0] op_sel_hi:[0,1]
	v_and_b32_e32 v127, 0xffff0000, v70
	v_lshlrev_b32_e32 v130, 16, v61
	v_and_b32_e32 v61, 0xffff0000, v71
	v_pk_mul_f32 v[70:71], v[58:59], v[134:135] op_sel:[1,0] op_sel_hi:[0,1]
	v_pk_mul_f32 v[128:129], v[58:59], v[128:129] op_sel:[1,0] op_sel_hi:[0,1]
	v_pk_mul_f32 v[58:59], v[58:59], v[62:63] op_sel:[1,0] op_sel_hi:[0,1]
	v_pk_fma_f32 v[62:63], v[56:57], v[136:137], v[68:69] op_sel:[1,0,0] op_sel_hi:[0,1,1]
	v_add_f32_e32 v116, v132, v116
	v_pk_fma_f32 v[68:69], v[56:57], v[130:131], v[70:71] op_sel:[1,0,0] op_sel_hi:[0,1,1]
	v_pk_fma_f32 v[58:59], v[56:57], v[60:61], v[58:59] op_sel:[1,0,0] op_sel_hi:[0,1,1]
	s_waitcnt lgkmcnt(1)
	v_pk_fma_f32 v[60:61], v[138:139], v[62:63], v[150:151]
	v_pk_fma_f32 v[62:63], v[140:141], v[68:69], v[152:153]
	v_pk_mul_f32 v[68:69], v[60:61], v[60:61]
	v_add_f32_e32 v116, v133, v116
	v_pk_fma_f32 v[70:71], v[56:57], v[126:127], v[128:129] op_sel:[1,0,0] op_sel_hi:[0,1,1]
	v_add_f32_e32 v68, v68, v116
	s_waitcnt lgkmcnt(0)
	v_pk_fma_f32 v[56:57], v[142:143], v[70:71], v[146:147]
	v_pk_mul_f32 v[70:71], v[62:63], v[62:63]
	v_add_f32_e32 v68, v69, v68
	v_add_f32_e32 v68, v70, v68
	v_pk_mul_f32 v[126:127], v[56:57], v[56:57]
	v_add_f32_e32 v68, v71, v68
	v_pk_fma_f32 v[58:59], v[144:145], v[58:59], v[148:149]
	v_add_f32_e32 v68, v126, v68
	v_pk_mul_f32 v[128:129], v[58:59], v[58:59]
	v_add_f32_e32 v68, v127, v68
	v_add_f32_e32 v68, v128, v68
	v_add_f32_e32 v68, v129, v68
	ds_bpermute_b32 v69, v168, v68
	global_store_dwordx4 v[66:67], v[60:63], off offset:896
	global_store_dwordx4 v[66:67], v[56:59], off offset:912
	s_waitcnt lgkmcnt(0)
	v_add_f32_e32 v68, v68, v69
	ds_bpermute_b32 v69, v169, v68
	s_and_saveexec_b64 s[6:7], s[0:1]
	s_cbranch_execz .LBB0_1312
	s_waitcnt lgkmcnt(0)
	v_add_f32_e32 v66, v68, v69
	v_add_u32_e32 v67, s23, v170
	ds_write_b32 v67, v66
